# GDN chunk-local phase step 4: (I+L)^-1 by 2x2 block scheme on all 8 waves (two half-wave 32-row substitutions, then X=L21*T11 and T21=-T22*X as f32 FMA matmuls) instead of one 64-row substitution on 2
# speedup vs baseline: 1.0128x; 1.0128x over previous
.LBB0_1574:
	s_or_b64 exec, exec, s[0:1]
	s_waitcnt lgkmcnt(0)
	s_barrier
	s_cmp_gt_u32 s10, 1
	s_cbranch_scc1 .Lg4_s1done
	v_lshrrev_b32_e32 v4, 5, v21
	v_and_b32_e32 v108, 31, v21
	s_mul_i32 s1, s10, 0x4800
	v_mul_u32_u24_e32 v5, 0x2280, v4
	s_mul_i32 s11, s10, 0x3000
	v_lshlrev_b32_e32 v6, 12, v4
	v_add3_u32 v109, v61, v5, s1
	s_add_i32 s11, s11, 0x1b000
	v_lshl_add_u32 v6, v108, 2, v6
	v_add3_u32 v1, v61, v6, s11
	v_cmp_eq_u32_e32 vcc, 0, v108
	ds_read_b128 v[168:171], v109 offset:272
	s_nop 0
	v_cndmask_b32_e64 v72, 0, 1.0, vcc
	v_cmp_eq_u32_e32 vcc, 1, v108
	ds_read_b128 v[136:139], v109 offset:544
	s_nop 0
	s_waitcnt lgkmcnt(1)
	v_cndmask_b32_e64 v104, 0, 1.0, vcc
	v_fma_f32 v104, -v168, v72, v104
	v_mov_b32_e32 v73, v104
	v_cmp_eq_u32_e32 vcc, 2, v108
	ds_read_b128 v[168:171], v109 offset:816
	s_nop 0
	s_waitcnt lgkmcnt(1)
	v_cndmask_b32_e64 v104, 0, 1.0, vcc
	v_fma_f32 v104, -v136, v72, v104
	v_mul_f32_e64 v105, -v137, v73
	v_add_f32_e32 v74, v104, v105
	v_cmp_eq_u32_e32 vcc, 3, v108
	ds_read_b128 v[136:139], v109 offset:1088
	s_nop 0
	s_waitcnt lgkmcnt(1)
	v_cndmask_b32_e64 v104, 0, 1.0, vcc
	v_fma_f32 v104, -v168, v72, v104
	v_mul_f32_e64 v105, -v169, v73
	v_mul_f32_e64 v106, -v170, v74
	v_add_f32_e32 v104, v104, v105
	v_add_f32_e32 v75, v104, v106
	v_cmp_eq_u32_e32 vcc, 4, v108
	ds_read_b128 v[168:171], v109 offset:1360
	ds_read_b128 v[172:175], v109 offset:1376
	s_waitcnt lgkmcnt(2)
	v_cndmask_b32_e64 v104, 0, 1.0, vcc
	v_fma_f32 v104, -v136, v72, v104
	v_mul_f32_e64 v105, -v137, v73
	v_mul_f32_e64 v106, -v138, v74
	v_mul_f32_e64 v107, -v139, v75
	v_add_f32_e32 v104, v104, v105
	v_add_f32_e32 v106, v106, v107
	v_add_f32_e32 v76, v104, v106
	v_cmp_eq_u32_e32 vcc, 5, v108
	ds_read_b128 v[136:139], v109 offset:1632
	ds_read_b128 v[140:143], v109 offset:1648
	s_waitcnt lgkmcnt(2)
	v_cndmask_b32_e64 v104, 0, 1.0, vcc
	v_fma_f32 v104, -v168, v72, v104
	v_mul_f32_e64 v105, -v169, v73
	v_mul_f32_e64 v106, -v170, v74
	v_mul_f32_e64 v107, -v171, v75
	v_fma_f32 v104, -v172, v76, v104
	v_add_f32_e32 v104, v104, v105
	v_add_f32_e32 v106, v106, v107
	v_add_f32_e32 v77, v104, v106
	v_cmp_eq_u32_e32 vcc, 6, v108
	ds_read_b128 v[168:171], v109 offset:1904
	ds_read_b128 v[172:175], v109 offset:1920
	s_waitcnt lgkmcnt(2)
	v_cndmask_b32_e64 v104, 0, 1.0, vcc
	v_fma_f32 v104, -v136, v72, v104
	v_mul_f32_e64 v105, -v137, v73
	v_mul_f32_e64 v106, -v138, v74
	v_mul_f32_e64 v107, -v139, v75
	v_fma_f32 v104, -v140, v76, v104
	v_fma_f32 v105, -v141, v77, v105
	v_add_f32_e32 v104, v104, v105
	v_add_f32_e32 v106, v106, v107
	v_add_f32_e32 v78, v104, v106
	v_cmp_eq_u32_e32 vcc, 7, v108
	ds_read_b128 v[136:139], v109 offset:2176
	ds_read_b128 v[140:143], v109 offset:2192
	s_waitcnt lgkmcnt(2)
	v_cndmask_b32_e64 v104, 0, 1.0, vcc
	v_fma_f32 v104, -v168, v72, v104
	v_mul_f32_e64 v105, -v169, v73
	v_mul_f32_e64 v106, -v170, v74
	v_mul_f32_e64 v107, -v171, v75
	v_fma_f32 v104, -v172, v76, v104
	v_fma_f32 v105, -v173, v77, v105
	v_fma_f32 v106, -v174, v78, v106
	v_add_f32_e32 v104, v104, v105
	v_add_f32_e32 v106, v106, v107
	v_add_f32_e32 v79, v104, v106
	v_cmp_eq_u32_e32 vcc, 8, v108
	ds_read_b128 v[168:171], v109 offset:2448
	ds_read_b128 v[172:175], v109 offset:2464
	ds_read_b128 v[176:179], v109 offset:2480
	s_waitcnt lgkmcnt(3)
	v_cndmask_b32_e64 v104, 0, 1.0, vcc
	v_fma_f32 v104, -v136, v72, v104
	v_mul_f32_e64 v105, -v137, v73
	v_mul_f32_e64 v106, -v138, v74
	v_mul_f32_e64 v107, -v139, v75
	v_fma_f32 v104, -v140, v76, v104
	v_fma_f32 v105, -v141, v77, v105
	v_fma_f32 v106, -v142, v78, v106
	v_fma_f32 v107, -v143, v79, v107
	v_add_f32_e32 v104, v104, v105
	v_add_f32_e32 v106, v106, v107
	v_add_f32_e32 v80, v104, v106
	v_cmp_eq_u32_e32 vcc, 9, v108
	ds_read_b128 v[136:139], v109 offset:2720
	ds_read_b128 v[140:143], v109 offset:2736
	ds_read_b128 v[144:147], v109 offset:2752
	s_waitcnt lgkmcnt(3)
	v_cndmask_b32_e64 v104, 0, 1.0, vcc
	v_fma_f32 v104, -v168, v72, v104
	v_mul_f32_e64 v105, -v169, v73
	v_mul_f32_e64 v106, -v170, v74
	v_mul_f32_e64 v107, -v171, v75
	v_fma_f32 v104, -v172, v76, v104
	v_fma_f32 v105, -v173, v77, v105
	v_fma_f32 v106, -v174, v78, v106
	v_fma_f32 v107, -v175, v79, v107
	v_fma_f32 v104, -v176, v80, v104
	v_add_f32_e32 v104, v104, v105
	v_add_f32_e32 v106, v106, v107
	v_add_f32_e32 v81, v104, v106
	v_cmp_eq_u32_e32 vcc, 10, v108
	ds_read_b128 v[168:171], v109 offset:2992
	ds_read_b128 v[172:175], v109 offset:3008
	ds_read_b128 v[176:179], v109 offset:3024
	s_waitcnt lgkmcnt(3)
	v_cndmask_b32_e64 v104, 0, 1.0, vcc
	v_fma_f32 v104, -v136, v72, v104
	v_mul_f32_e64 v105, -v137, v73
	v_mul_f32_e64 v106, -v138, v74
	v_mul_f32_e64 v107, -v139, v75
	v_fma_f32 v104, -v140, v76, v104
	v_fma_f32 v105, -v141, v77, v105
	v_fma_f32 v106, -v142, v78, v106
	v_fma_f32 v107, -v143, v79, v107
	v_fma_f32 v104, -v144, v80, v104
	v_fma_f32 v105, -v145, v81, v105
	v_add_f32_e32 v104, v104, v105
	v_add_f32_e32 v106, v106, v107
	v_add_f32_e32 v82, v104, v106
	v_cmp_eq_u32_e32 vcc, 11, v108
	ds_read_b128 v[136:139], v109 offset:3264
	ds_read_b128 v[140:143], v109 offset:3280
	ds_read_b128 v[144:147], v109 offset:3296
	s_waitcnt lgkmcnt(3)
	v_cndmask_b32_e64 v104, 0, 1.0, vcc
	v_fma_f32 v104, -v168, v72, v104
	v_mul_f32_e64 v105, -v169, v73
	v_mul_f32_e64 v106, -v170, v74
	v_mul_f32_e64 v107, -v171, v75
	v_fma_f32 v104, -v172, v76, v104
	v_fma_f32 v105, -v173, v77, v105
	v_fma_f32 v106, -v174, v78, v106
	v_fma_f32 v107, -v175, v79, v107
	v_fma_f32 v104, -v176, v80, v104
	v_fma_f32 v105, -v177, v81, v105
	v_fma_f32 v106, -v178, v82, v106
	v_add_f32_e32 v104, v104, v105
	v_add_f32_e32 v106, v106, v107
	v_add_f32_e32 v83, v104, v106
	v_cmp_eq_u32_e32 vcc, 12, v108
	ds_read_b128 v[168:171], v109 offset:3536
	ds_read_b128 v[172:175], v109 offset:3552
	ds_read_b128 v[176:179], v109 offset:3568
	ds_read_b128 v[180:183], v109 offset:3584
	s_waitcnt lgkmcnt(4)
	v_cndmask_b32_e64 v104, 0, 1.0, vcc
	v_fma_f32 v104, -v136, v72, v104
	v_mul_f32_e64 v105, -v137, v73
	v_mul_f32_e64 v106, -v138, v74
	v_mul_f32_e64 v107, -v139, v75
	v_fma_f32 v104, -v140, v76, v104
	v_fma_f32 v105, -v141, v77, v105
	v_fma_f32 v106, -v142, v78, v106
	v_fma_f32 v107, -v143, v79, v107
	v_fma_f32 v104, -v144, v80, v104
	v_fma_f32 v105, -v145, v81, v105
	v_fma_f32 v106, -v146, v82, v106
	v_fma_f32 v107, -v147, v83, v107
	v_add_f32_e32 v104, v104, v105
	v_add_f32_e32 v106, v106, v107
	v_add_f32_e32 v84, v104, v106
	v_cmp_eq_u32_e32 vcc, 13, v108
	ds_read_b128 v[136:139], v109 offset:3808
	ds_read_b128 v[140:143], v109 offset:3824
	ds_read_b128 v[144:147], v109 offset:3840
	ds_read_b128 v[148:151], v109 offset:3856
	s_waitcnt lgkmcnt(4)
	v_cndmask_b32_e64 v104, 0, 1.0, vcc
	v_fma_f32 v104, -v168, v72, v104
	v_mul_f32_e64 v105, -v169, v73
	v_mul_f32_e64 v106, -v170, v74
	v_mul_f32_e64 v107, -v171, v75
	v_fma_f32 v104, -v172, v76, v104
	v_fma_f32 v105, -v173, v77, v105
	v_fma_f32 v106, -v174, v78, v106
	v_fma_f32 v107, -v175, v79, v107
	v_fma_f32 v104, -v176, v80, v104
	v_fma_f32 v105, -v177, v81, v105
	v_fma_f32 v106, -v178, v82, v106
	v_fma_f32 v107, -v179, v83, v107
	v_fma_f32 v104, -v180, v84, v104
	v_add_f32_e32 v104, v104, v105
	v_add_f32_e32 v106, v106, v107
	v_add_f32_e32 v85, v104, v106
	v_cmp_eq_u32_e32 vcc, 14, v108
	ds_read_b128 v[168:171], v109 offset:4080
	ds_read_b128 v[172:175], v109 offset:4096
	ds_read_b128 v[176:179], v109 offset:4112
	ds_read_b128 v[180:183], v109 offset:4128
	s_waitcnt lgkmcnt(4)
	v_cndmask_b32_e64 v104, 0, 1.0, vcc
	v_fma_f32 v104, -v136, v72, v104
	v_mul_f32_e64 v105, -v137, v73
	v_mul_f32_e64 v106, -v138, v74
	v_mul_f32_e64 v107, -v139, v75
	v_fma_f32 v104, -v140, v76, v104
	v_fma_f32 v105, -v141, v77, v105
	v_fma_f32 v106, -v142, v78, v106
	v_fma_f32 v107, -v143, v79, v107
	v_fma_f32 v104, -v144, v80, v104
	v_fma_f32 v105, -v145, v81, v105
	v_fma_f32 v106, -v146, v82, v106
	v_fma_f32 v107, -v147, v83, v107
	v_fma_f32 v104, -v148, v84, v104
	v_fma_f32 v105, -v149, v85, v105
	v_add_f32_e32 v104, v104, v105
	v_add_f32_e32 v106, v106, v107
	v_add_f32_e32 v86, v104, v106
	v_cmp_eq_u32_e32 vcc, 15, v108
	ds_read_b128 v[136:139], v109 offset:4352
	ds_read_b128 v[140:143], v109 offset:4368
	ds_read_b128 v[144:147], v109 offset:4384
	ds_read_b128 v[148:151], v109 offset:4400
	s_waitcnt lgkmcnt(4)
	v_cndmask_b32_e64 v104, 0, 1.0, vcc
	v_fma_f32 v104, -v168, v72, v104
	v_mul_f32_e64 v105, -v169, v73
	v_mul_f32_e64 v106, -v170, v74
	v_mul_f32_e64 v107, -v171, v75
	v_fma_f32 v104, -v172, v76, v104
	v_fma_f32 v105, -v173, v77, v105
	v_fma_f32 v106, -v174, v78, v106
	v_fma_f32 v107, -v175, v79, v107
	v_fma_f32 v104, -v176, v80, v104
	v_fma_f32 v105, -v177, v81, v105
	v_fma_f32 v106, -v178, v82, v106
	v_fma_f32 v107, -v179, v83, v107
	v_fma_f32 v104, -v180, v84, v104
	v_fma_f32 v105, -v181, v85, v105
	v_fma_f32 v106, -v182, v86, v106
	v_add_f32_e32 v104, v104, v105
	v_add_f32_e32 v106, v106, v107
	v_add_f32_e32 v87, v104, v106
	v_cmp_eq_u32_e32 vcc, 16, v108
	ds_read_b128 v[168:171], v109 offset:4624
	ds_read_b128 v[172:175], v109 offset:4640
	ds_read_b128 v[176:179], v109 offset:4656
	ds_read_b128 v[180:183], v109 offset:4672
	ds_read_b128 v[184:187], v109 offset:4688
	s_waitcnt lgkmcnt(5)
	v_cndmask_b32_e64 v104, 0, 1.0, vcc
	v_fma_f32 v104, -v136, v72, v104
	v_mul_f32_e64 v105, -v137, v73
	v_mul_f32_e64 v106, -v138, v74
	v_mul_f32_e64 v107, -v139, v75
	v_fma_f32 v104, -v140, v76, v104
	v_fma_f32 v105, -v141, v77, v105
	v_fma_f32 v106, -v142, v78, v106
	v_fma_f32 v107, -v143, v79, v107
	v_fma_f32 v104, -v144, v80, v104
	v_fma_f32 v105, -v145, v81, v105
	v_fma_f32 v106, -v146, v82, v106
	v_fma_f32 v107, -v147, v83, v107
	v_fma_f32 v104, -v148, v84, v104
	v_fma_f32 v105, -v149, v85, v105
	v_fma_f32 v106, -v150, v86, v106
	v_fma_f32 v107, -v151, v87, v107
	v_add_f32_e32 v104, v104, v105
	v_add_f32_e32 v106, v106, v107
	v_add_f32_e32 v88, v104, v106
	v_cmp_eq_u32_e32 vcc, 17, v108
	ds_read_b128 v[136:139], v109 offset:4896
	ds_read_b128 v[140:143], v109 offset:4912
	ds_read_b128 v[144:147], v109 offset:4928
	ds_read_b128 v[148:151], v109 offset:4944
	ds_read_b128 v[152:155], v109 offset:4960
	s_waitcnt lgkmcnt(5)
	v_cndmask_b32_e64 v104, 0, 1.0, vcc
	v_fma_f32 v104, -v168, v72, v104
	v_mul_f32_e64 v105, -v169, v73
	v_mul_f32_e64 v106, -v170, v74
	v_mul_f32_e64 v107, -v171, v75
	v_fma_f32 v104, -v172, v76, v104
	v_fma_f32 v105, -v173, v77, v105
	v_fma_f32 v106, -v174, v78, v106
	v_fma_f32 v107, -v175, v79, v107
	v_fma_f32 v104, -v176, v80, v104
	v_fma_f32 v105, -v177, v81, v105
	v_fma_f32 v106, -v178, v82, v106
	v_fma_f32 v107, -v179, v83, v107
	v_fma_f32 v104, -v180, v84, v104
	v_fma_f32 v105, -v181, v85, v105
	v_fma_f32 v106, -v182, v86, v106
	v_fma_f32 v107, -v183, v87, v107
	v_fma_f32 v104, -v184, v88, v104
	v_add_f32_e32 v104, v104, v105
	v_add_f32_e32 v106, v106, v107
	v_add_f32_e32 v89, v104, v106
	v_cmp_eq_u32_e32 vcc, 18, v108
	ds_read_b128 v[168:171], v109 offset:5168
	ds_read_b128 v[172:175], v109 offset:5184
	ds_read_b128 v[176:179], v109 offset:5200
	ds_read_b128 v[180:183], v109 offset:5216
	ds_read_b128 v[184:187], v109 offset:5232
	s_waitcnt lgkmcnt(5)
	v_cndmask_b32_e64 v104, 0, 1.0, vcc
	v_fma_f32 v104, -v136, v72, v104
	v_mul_f32_e64 v105, -v137, v73
	v_mul_f32_e64 v106, -v138, v74
	v_mul_f32_e64 v107, -v139, v75
	v_fma_f32 v104, -v140, v76, v104
	v_fma_f32 v105, -v141, v77, v105
	v_fma_f32 v106, -v142, v78, v106
	v_fma_f32 v107, -v143, v79, v107
	v_fma_f32 v104, -v144, v80, v104
	v_fma_f32 v105, -v145, v81, v105
	v_fma_f32 v106, -v146, v82, v106
	v_fma_f32 v107, -v147, v83, v107
	v_fma_f32 v104, -v148, v84, v104
	v_fma_f32 v105, -v149, v85, v105
	v_fma_f32 v106, -v150, v86, v106
	v_fma_f32 v107, -v151, v87, v107
	v_fma_f32 v104, -v152, v88, v104
	v_fma_f32 v105, -v153, v89, v105
	v_add_f32_e32 v104, v104, v105
	v_add_f32_e32 v106, v106, v107
	v_add_f32_e32 v90, v104, v106
	v_cmp_eq_u32_e32 vcc, 19, v108
	ds_read_b128 v[136:139], v109 offset:5440
	ds_read_b128 v[140:143], v109 offset:5456
	ds_read_b128 v[144:147], v109 offset:5472
	ds_read_b128 v[148:151], v109 offset:5488
	ds_read_b128 v[152:155], v109 offset:5504
	s_waitcnt lgkmcnt(5)
	v_cndmask_b32_e64 v104, 0, 1.0, vcc
	v_fma_f32 v104, -v168, v72, v104
	v_mul_f32_e64 v105, -v169, v73
	v_mul_f32_e64 v106, -v170, v74
	v_mul_f32_e64 v107, -v171, v75
	v_fma_f32 v104, -v172, v76, v104
	v_fma_f32 v105, -v173, v77, v105
	v_fma_f32 v106, -v174, v78, v106
	v_fma_f32 v107, -v175, v79, v107
	v_fma_f32 v104, -v176, v80, v104
	v_fma_f32 v105, -v177, v81, v105
	v_fma_f32 v106, -v178, v82, v106
	v_fma_f32 v107, -v179, v83, v107
	v_fma_f32 v104, -v180, v84, v104
	v_fma_f32 v105, -v181, v85, v105
	v_fma_f32 v106, -v182, v86, v106
	v_fma_f32 v107, -v183, v87, v107
	v_fma_f32 v104, -v184, v88, v104
	v_fma_f32 v105, -v185, v89, v105
	v_fma_f32 v106, -v186, v90, v106
	v_add_f32_e32 v104, v104, v105
	v_add_f32_e32 v106, v106, v107
	v_add_f32_e32 v91, v104, v106
	v_cmp_eq_u32_e32 vcc, 20, v108
	ds_read_b128 v[168:171], v109 offset:5712
	ds_read_b128 v[172:175], v109 offset:5728
	ds_read_b128 v[176:179], v109 offset:5744
	ds_read_b128 v[180:183], v109 offset:5760
	ds_read_b128 v[184:187], v109 offset:5776
	ds_read_b128 v[188:191], v109 offset:5792
	s_waitcnt lgkmcnt(6)
	v_cndmask_b32_e64 v104, 0, 1.0, vcc
	v_fma_f32 v104, -v136, v72, v104
	v_mul_f32_e64 v105, -v137, v73
	v_mul_f32_e64 v106, -v138, v74
	v_mul_f32_e64 v107, -v139, v75
	v_fma_f32 v104, -v140, v76, v104
	v_fma_f32 v105, -v141, v77, v105
	v_fma_f32 v106, -v142, v78, v106
	v_fma_f32 v107, -v143, v79, v107
	v_fma_f32 v104, -v144, v80, v104
	v_fma_f32 v105, -v145, v81, v105
	v_fma_f32 v106, -v146, v82, v106
	v_fma_f32 v107, -v147, v83, v107
	v_fma_f32 v104, -v148, v84, v104
	v_fma_f32 v105, -v149, v85, v105
	v_fma_f32 v106, -v150, v86, v106
	v_fma_f32 v107, -v151, v87, v107
	v_fma_f32 v104, -v152, v88, v104
	v_fma_f32 v105, -v153, v89, v105
	v_fma_f32 v106, -v154, v90, v106
	v_fma_f32 v107, -v155, v91, v107
	v_add_f32_e32 v104, v104, v105
	v_add_f32_e32 v106, v106, v107
	v_add_f32_e32 v92, v104, v106
	v_cmp_eq_u32_e32 vcc, 21, v108
	ds_read_b128 v[136:139], v109 offset:5984
	ds_read_b128 v[140:143], v109 offset:6000
	ds_read_b128 v[144:147], v109 offset:6016
	ds_read_b128 v[148:151], v109 offset:6032
	ds_read_b128 v[152:155], v109 offset:6048
	ds_read_b128 v[156:159], v109 offset:6064
	s_waitcnt lgkmcnt(6)
	v_cndmask_b32_e64 v104, 0, 1.0, vcc
	v_fma_f32 v104, -v168, v72, v104
	v_mul_f32_e64 v105, -v169, v73
	v_mul_f32_e64 v106, -v170, v74
	v_mul_f32_e64 v107, -v171, v75
	v_fma_f32 v104, -v172, v76, v104
	v_fma_f32 v105, -v173, v77, v105
	v_fma_f32 v106, -v174, v78, v106
	v_fma_f32 v107, -v175, v79, v107
	v_fma_f32 v104, -v176, v80, v104
	v_fma_f32 v105, -v177, v81, v105
	v_fma_f32 v106, -v178, v82, v106
	v_fma_f32 v107, -v179, v83, v107
	v_fma_f32 v104, -v180, v84, v104
	v_fma_f32 v105, -v181, v85, v105
	v_fma_f32 v106, -v182, v86, v106
	v_fma_f32 v107, -v183, v87, v107
	v_fma_f32 v104, -v184, v88, v104
	v_fma_f32 v105, -v185, v89, v105
	v_fma_f32 v106, -v186, v90, v106
	v_fma_f32 v107, -v187, v91, v107
	v_fma_f32 v104, -v188, v92, v104
	v_add_f32_e32 v104, v104, v105
	v_add_f32_e32 v106, v106, v107
	v_add_f32_e32 v93, v104, v106
	v_cmp_eq_u32_e32 vcc, 22, v108
	ds_read_b128 v[168:171], v109 offset:6256
	ds_read_b128 v[172:175], v109 offset:6272
	ds_read_b128 v[176:179], v109 offset:6288
	ds_read_b128 v[180:183], v109 offset:6304
	ds_read_b128 v[184:187], v109 offset:6320
	ds_read_b128 v[188:191], v109 offset:6336
	s_waitcnt lgkmcnt(6)
	v_cndmask_b32_e64 v104, 0, 1.0, vcc
	v_fma_f32 v104, -v136, v72, v104
	v_mul_f32_e64 v105, -v137, v73
	v_mul_f32_e64 v106, -v138, v74
	v_mul_f32_e64 v107, -v139, v75
	v_fma_f32 v104, -v140, v76, v104
	v_fma_f32 v105, -v141, v77, v105
	v_fma_f32 v106, -v142, v78, v106
	v_fma_f32 v107, -v143, v79, v107
	v_fma_f32 v104, -v144, v80, v104
	v_fma_f32 v105, -v145, v81, v105
	v_fma_f32 v106, -v146, v82, v106
	v_fma_f32 v107, -v147, v83, v107
	v_fma_f32 v104, -v148, v84, v104
	v_fma_f32 v105, -v149, v85, v105
	v_fma_f32 v106, -v150, v86, v106
	v_fma_f32 v107, -v151, v87, v107
	v_fma_f32 v104, -v152, v88, v104
	v_fma_f32 v105, -v153, v89, v105
	v_fma_f32 v106, -v154, v90, v106
	v_fma_f32 v107, -v155, v91, v107
	v_fma_f32 v104, -v156, v92, v104
	v_fma_f32 v105, -v157, v93, v105
	v_add_f32_e32 v104, v104, v105
	v_add_f32_e32 v106, v106, v107
	v_add_f32_e32 v94, v104, v106
	v_cmp_eq_u32_e32 vcc, 23, v108
	ds_read_b128 v[136:139], v109 offset:6528
	ds_read_b128 v[140:143], v109 offset:6544
	ds_read_b128 v[144:147], v109 offset:6560
	ds_read_b128 v[148:151], v109 offset:6576
	ds_read_b128 v[152:155], v109 offset:6592
	ds_read_b128 v[156:159], v109 offset:6608
	s_waitcnt lgkmcnt(6)
	v_cndmask_b32_e64 v104, 0, 1.0, vcc
	v_fma_f32 v104, -v168, v72, v104
	v_mul_f32_e64 v105, -v169, v73
	v_mul_f32_e64 v106, -v170, v74
	v_mul_f32_e64 v107, -v171, v75
	v_fma_f32 v104, -v172, v76, v104
	v_fma_f32 v105, -v173, v77, v105
	v_fma_f32 v106, -v174, v78, v106
	v_fma_f32 v107, -v175, v79, v107
	v_fma_f32 v104, -v176, v80, v104
	v_fma_f32 v105, -v177, v81, v105
	v_fma_f32 v106, -v178, v82, v106
	v_fma_f32 v107, -v179, v83, v107
	v_fma_f32 v104, -v180, v84, v104
	v_fma_f32 v105, -v181, v85, v105
	v_fma_f32 v106, -v182, v86, v106
	v_fma_f32 v107, -v183, v87, v107
	v_fma_f32 v104, -v184, v88, v104
	v_fma_f32 v105, -v185, v89, v105
	v_fma_f32 v106, -v186, v90, v106
	v_fma_f32 v107, -v187, v91, v107
	v_fma_f32 v104, -v188, v92, v104
	v_fma_f32 v105, -v189, v93, v105
	v_fma_f32 v106, -v190, v94, v106
	v_add_f32_e32 v104, v104, v105
	v_add_f32_e32 v106, v106, v107
	v_add_f32_e32 v95, v104, v106
	v_cmp_eq_u32_e32 vcc, 24, v108
	ds_read_b128 v[168:171], v109 offset:6800
	ds_read_b128 v[172:175], v109 offset:6816
	ds_read_b128 v[176:179], v109 offset:6832
	ds_read_b128 v[180:183], v109 offset:6848
	ds_read_b128 v[184:187], v109 offset:6864
	ds_read_b128 v[188:191], v109 offset:6880
	ds_read_b128 v[192:195], v109 offset:6896
	s_waitcnt lgkmcnt(7)
	v_cndmask_b32_e64 v104, 0, 1.0, vcc
	v_fma_f32 v104, -v136, v72, v104
	v_mul_f32_e64 v105, -v137, v73
	v_mul_f32_e64 v106, -v138, v74
	v_mul_f32_e64 v107, -v139, v75
	v_fma_f32 v104, -v140, v76, v104
	v_fma_f32 v105, -v141, v77, v105
	v_fma_f32 v106, -v142, v78, v106
	v_fma_f32 v107, -v143, v79, v107
	v_fma_f32 v104, -v144, v80, v104
	v_fma_f32 v105, -v145, v81, v105
	v_fma_f32 v106, -v146, v82, v106
	v_fma_f32 v107, -v147, v83, v107
	v_fma_f32 v104, -v148, v84, v104
	v_fma_f32 v105, -v149, v85, v105
	v_fma_f32 v106, -v150, v86, v106
	v_fma_f32 v107, -v151, v87, v107
	v_fma_f32 v104, -v152, v88, v104
	v_fma_f32 v105, -v153, v89, v105
	v_fma_f32 v106, -v154, v90, v106
	v_fma_f32 v107, -v155, v91, v107
	v_fma_f32 v104, -v156, v92, v104
	v_fma_f32 v105, -v157, v93, v105
	v_fma_f32 v106, -v158, v94, v106
	v_fma_f32 v107, -v159, v95, v107
	v_add_f32_e32 v104, v104, v105
	v_add_f32_e32 v106, v106, v107
	v_add_f32_e32 v96, v104, v106
	v_cmp_eq_u32_e32 vcc, 25, v108
	ds_read_b128 v[136:139], v109 offset:7072
	ds_read_b128 v[140:143], v109 offset:7088
	ds_read_b128 v[144:147], v109 offset:7104
	ds_read_b128 v[148:151], v109 offset:7120
	ds_read_b128 v[152:155], v109 offset:7136
	ds_read_b128 v[156:159], v109 offset:7152
	ds_read_b128 v[160:163], v109 offset:7168
	s_waitcnt lgkmcnt(7)
	v_cndmask_b32_e64 v104, 0, 1.0, vcc
	v_fma_f32 v104, -v168, v72, v104
	v_mul_f32_e64 v105, -v169, v73
	v_mul_f32_e64 v106, -v170, v74
	v_mul_f32_e64 v107, -v171, v75
	v_fma_f32 v104, -v172, v76, v104
	v_fma_f32 v105, -v173, v77, v105
	v_fma_f32 v106, -v174, v78, v106
	v_fma_f32 v107, -v175, v79, v107
	v_fma_f32 v104, -v176, v80, v104
	v_fma_f32 v105, -v177, v81, v105
	v_fma_f32 v106, -v178, v82, v106
	v_fma_f32 v107, -v179, v83, v107
	v_fma_f32 v104, -v180, v84, v104
	v_fma_f32 v105, -v181, v85, v105
	v_fma_f32 v106, -v182, v86, v106
	v_fma_f32 v107, -v183, v87, v107
	v_fma_f32 v104, -v184, v88, v104
	v_fma_f32 v105, -v185, v89, v105
	v_fma_f32 v106, -v186, v90, v106
	v_fma_f32 v107, -v187, v91, v107
	v_fma_f32 v104, -v188, v92, v104
	v_fma_f32 v105, -v189, v93, v105
	v_fma_f32 v106, -v190, v94, v106
	v_fma_f32 v107, -v191, v95, v107
	v_fma_f32 v104, -v192, v96, v104
	v_add_f32_e32 v104, v104, v105
	v_add_f32_e32 v106, v106, v107
	v_add_f32_e32 v97, v104, v106
	v_cmp_eq_u32_e32 vcc, 26, v108
	ds_read_b128 v[168:171], v109 offset:7344
	ds_read_b128 v[172:175], v109 offset:7360
	ds_read_b128 v[176:179], v109 offset:7376
	ds_read_b128 v[180:183], v109 offset:7392
	ds_read_b128 v[184:187], v109 offset:7408
	ds_read_b128 v[188:191], v109 offset:7424
	ds_read_b128 v[192:195], v109 offset:7440
	s_waitcnt lgkmcnt(7)
	v_cndmask_b32_e64 v104, 0, 1.0, vcc
	v_fma_f32 v104, -v136, v72, v104
	v_mul_f32_e64 v105, -v137, v73
	v_mul_f32_e64 v106, -v138, v74
	v_mul_f32_e64 v107, -v139, v75
	v_fma_f32 v104, -v140, v76, v104
	v_fma_f32 v105, -v141, v77, v105
	v_fma_f32 v106, -v142, v78, v106
	v_fma_f32 v107, -v143, v79, v107
	v_fma_f32 v104, -v144, v80, v104
	v_fma_f32 v105, -v145, v81, v105
	v_fma_f32 v106, -v146, v82, v106
	v_fma_f32 v107, -v147, v83, v107
	v_fma_f32 v104, -v148, v84, v104
	v_fma_f32 v105, -v149, v85, v105
	v_fma_f32 v106, -v150, v86, v106
	v_fma_f32 v107, -v151, v87, v107
	v_fma_f32 v104, -v152, v88, v104
	v_fma_f32 v105, -v153, v89, v105
	v_fma_f32 v106, -v154, v90, v106
	v_fma_f32 v107, -v155, v91, v107
	v_fma_f32 v104, -v156, v92, v104
	v_fma_f32 v105, -v157, v93, v105
	v_fma_f32 v106, -v158, v94, v106
	v_fma_f32 v107, -v159, v95, v107
	v_fma_f32 v104, -v160, v96, v104
	v_fma_f32 v105, -v161, v97, v105
	v_add_f32_e32 v104, v104, v105
	v_add_f32_e32 v106, v106, v107
	v_add_f32_e32 v98, v104, v106
	v_cmp_eq_u32_e32 vcc, 27, v108
	ds_read_b128 v[136:139], v109 offset:7616
	ds_read_b128 v[140:143], v109 offset:7632
	ds_read_b128 v[144:147], v109 offset:7648
	ds_read_b128 v[148:151], v109 offset:7664
	ds_read_b128 v[152:155], v109 offset:7680
	ds_read_b128 v[156:159], v109 offset:7696
	ds_read_b128 v[160:163], v109 offset:7712
	s_waitcnt lgkmcnt(7)
	v_cndmask_b32_e64 v104, 0, 1.0, vcc
	v_fma_f32 v104, -v168, v72, v104
	v_mul_f32_e64 v105, -v169, v73
	v_mul_f32_e64 v106, -v170, v74
	v_mul_f32_e64 v107, -v171, v75
	v_fma_f32 v104, -v172, v76, v104
	v_fma_f32 v105, -v173, v77, v105
	v_fma_f32 v106, -v174, v78, v106
	v_fma_f32 v107, -v175, v79, v107
	v_fma_f32 v104, -v176, v80, v104
	v_fma_f32 v105, -v177, v81, v105
	v_fma_f32 v106, -v178, v82, v106
	v_fma_f32 v107, -v179, v83, v107
	v_fma_f32 v104, -v180, v84, v104
	v_fma_f32 v105, -v181, v85, v105
	v_fma_f32 v106, -v182, v86, v106
	v_fma_f32 v107, -v183, v87, v107
	v_fma_f32 v104, -v184, v88, v104
	v_fma_f32 v105, -v185, v89, v105
	v_fma_f32 v106, -v186, v90, v106
	v_fma_f32 v107, -v187, v91, v107
	v_fma_f32 v104, -v188, v92, v104
	v_fma_f32 v105, -v189, v93, v105
	v_fma_f32 v106, -v190, v94, v106
	v_fma_f32 v107, -v191, v95, v107
	v_fma_f32 v104, -v192, v96, v104
	v_fma_f32 v105, -v193, v97, v105
	v_fma_f32 v106, -v194, v98, v106
	v_add_f32_e32 v104, v104, v105
	v_add_f32_e32 v106, v106, v107
	v_add_f32_e32 v99, v104, v106
	v_cmp_eq_u32_e32 vcc, 28, v108
	ds_read_b128 v[168:171], v109 offset:7888
	ds_read_b128 v[172:175], v109 offset:7904
	ds_read_b128 v[176:179], v109 offset:7920
	ds_read_b128 v[180:183], v109 offset:7936
	ds_read_b128 v[184:187], v109 offset:7952
	ds_read_b128 v[188:191], v109 offset:7968
	ds_read_b128 v[192:195], v109 offset:7984
	ds_read_b128 v[196:199], v109 offset:8000
	s_waitcnt lgkmcnt(8)
	v_cndmask_b32_e64 v104, 0, 1.0, vcc
	v_fma_f32 v104, -v136, v72, v104
	v_mul_f32_e64 v105, -v137, v73
	v_mul_f32_e64 v106, -v138, v74
	v_mul_f32_e64 v107, -v139, v75
	v_fma_f32 v104, -v140, v76, v104
	v_fma_f32 v105, -v141, v77, v105
	v_fma_f32 v106, -v142, v78, v106
	v_fma_f32 v107, -v143, v79, v107
	v_fma_f32 v104, -v144, v80, v104
	v_fma_f32 v105, -v145, v81, v105
	v_fma_f32 v106, -v146, v82, v106
	v_fma_f32 v107, -v147, v83, v107
	v_fma_f32 v104, -v148, v84, v104
	v_fma_f32 v105, -v149, v85, v105
	v_fma_f32 v106, -v150, v86, v106
	v_fma_f32 v107, -v151, v87, v107
	v_fma_f32 v104, -v152, v88, v104
	v_fma_f32 v105, -v153, v89, v105
	v_fma_f32 v106, -v154, v90, v106
	v_fma_f32 v107, -v155, v91, v107
	v_fma_f32 v104, -v156, v92, v104
	v_fma_f32 v105, -v157, v93, v105
	v_fma_f32 v106, -v158, v94, v106
	v_fma_f32 v107, -v159, v95, v107
	v_fma_f32 v104, -v160, v96, v104
	v_fma_f32 v105, -v161, v97, v105
	v_fma_f32 v106, -v162, v98, v106
	v_fma_f32 v107, -v163, v99, v107
	v_add_f32_e32 v104, v104, v105
	v_add_f32_e32 v106, v106, v107
	v_add_f32_e32 v100, v104, v106
	v_cmp_eq_u32_e32 vcc, 29, v108
	ds_read_b128 v[136:139], v109 offset:8160
	ds_read_b128 v[140:143], v109 offset:8176
	ds_read_b128 v[144:147], v109 offset:8192
	ds_read_b128 v[148:151], v109 offset:8208
	ds_read_b128 v[152:155], v109 offset:8224
	ds_read_b128 v[156:159], v109 offset:8240
	ds_read_b128 v[160:163], v109 offset:8256
	ds_read_b128 v[164:167], v109 offset:8272
	s_waitcnt lgkmcnt(8)
	v_cndmask_b32_e64 v104, 0, 1.0, vcc
	v_fma_f32 v104, -v168, v72, v104
	v_mul_f32_e64 v105, -v169, v73
	v_mul_f32_e64 v106, -v170, v74
	v_mul_f32_e64 v107, -v171, v75
	v_fma_f32 v104, -v172, v76, v104
	v_fma_f32 v105, -v173, v77, v105
	v_fma_f32 v106, -v174, v78, v106
	v_fma_f32 v107, -v175, v79, v107
	v_fma_f32 v104, -v176, v80, v104
	v_fma_f32 v105, -v177, v81, v105
	v_fma_f32 v106, -v178, v82, v106
	v_fma_f32 v107, -v179, v83, v107
	v_fma_f32 v104, -v180, v84, v104
	v_fma_f32 v105, -v181, v85, v105
	v_fma_f32 v106, -v182, v86, v106
	v_fma_f32 v107, -v183, v87, v107
	v_fma_f32 v104, -v184, v88, v104
	v_fma_f32 v105, -v185, v89, v105
	v_fma_f32 v106, -v186, v90, v106
	v_fma_f32 v107, -v187, v91, v107
	v_fma_f32 v104, -v188, v92, v104
	v_fma_f32 v105, -v189, v93, v105
	v_fma_f32 v106, -v190, v94, v106
	v_fma_f32 v107, -v191, v95, v107
	v_fma_f32 v104, -v192, v96, v104
	v_fma_f32 v105, -v193, v97, v105
	v_fma_f32 v106, -v194, v98, v106
	v_fma_f32 v107, -v195, v99, v107
	v_fma_f32 v104, -v196, v100, v104
	v_add_f32_e32 v104, v104, v105
	v_add_f32_e32 v106, v106, v107
	v_add_f32_e32 v101, v104, v106
	v_cmp_eq_u32_e32 vcc, 30, v108
	ds_read_b128 v[168:171], v109 offset:8432
	ds_read_b128 v[172:175], v109 offset:8448
	ds_read_b128 v[176:179], v109 offset:8464
	ds_read_b128 v[180:183], v109 offset:8480
	ds_read_b128 v[184:187], v109 offset:8496
	ds_read_b128 v[188:191], v109 offset:8512
	ds_read_b128 v[192:195], v109 offset:8528
	ds_read_b128 v[196:199], v109 offset:8544
	s_waitcnt lgkmcnt(8)
	v_cndmask_b32_e64 v104, 0, 1.0, vcc
	v_fma_f32 v104, -v136, v72, v104
	v_mul_f32_e64 v105, -v137, v73
	v_mul_f32_e64 v106, -v138, v74
	v_mul_f32_e64 v107, -v139, v75
	v_fma_f32 v104, -v140, v76, v104
	v_fma_f32 v105, -v141, v77, v105
	v_fma_f32 v106, -v142, v78, v106
	v_fma_f32 v107, -v143, v79, v107
	v_fma_f32 v104, -v144, v80, v104
	v_fma_f32 v105, -v145, v81, v105
	v_fma_f32 v106, -v146, v82, v106
	v_fma_f32 v107, -v147, v83, v107
	v_fma_f32 v104, -v148, v84, v104
	v_fma_f32 v105, -v149, v85, v105
	v_fma_f32 v106, -v150, v86, v106
	v_fma_f32 v107, -v151, v87, v107
	v_fma_f32 v104, -v152, v88, v104
	v_fma_f32 v105, -v153, v89, v105
	v_fma_f32 v106, -v154, v90, v106
	v_fma_f32 v107, -v155, v91, v107
	v_fma_f32 v104, -v156, v92, v104
	v_fma_f32 v105, -v157, v93, v105
	v_fma_f32 v106, -v158, v94, v106
	v_fma_f32 v107, -v159, v95, v107
	v_fma_f32 v104, -v160, v96, v104
	v_fma_f32 v105, -v161, v97, v105
	v_fma_f32 v106, -v162, v98, v106
	v_fma_f32 v107, -v163, v99, v107
	v_fma_f32 v104, -v164, v100, v104
	v_fma_f32 v105, -v165, v101, v105
	v_add_f32_e32 v104, v104, v105
	v_add_f32_e32 v106, v106, v107
	v_add_f32_e32 v102, v104, v106
	v_cmp_eq_u32_e32 vcc, 31, v108
	s_nop 1
	s_waitcnt lgkmcnt(0)
	v_cndmask_b32_e64 v104, 0, 1.0, vcc
	v_fma_f32 v104, -v168, v72, v104
	v_mul_f32_e64 v105, -v169, v73
	v_mul_f32_e64 v106, -v170, v74
	v_mul_f32_e64 v107, -v171, v75
	v_fma_f32 v104, -v172, v76, v104
	v_fma_f32 v105, -v173, v77, v105
	v_fma_f32 v106, -v174, v78, v106
	v_fma_f32 v107, -v175, v79, v107
	v_fma_f32 v104, -v176, v80, v104
	v_fma_f32 v105, -v177, v81, v105
	v_fma_f32 v106, -v178, v82, v106
	v_fma_f32 v107, -v179, v83, v107
	v_fma_f32 v104, -v180, v84, v104
	v_fma_f32 v105, -v181, v85, v105
	v_fma_f32 v106, -v182, v86, v106
	v_fma_f32 v107, -v183, v87, v107
	v_fma_f32 v104, -v184, v88, v104
	v_fma_f32 v105, -v185, v89, v105
	v_fma_f32 v106, -v186, v90, v106
	v_fma_f32 v107, -v187, v91, v107
	v_fma_f32 v104, -v188, v92, v104
	v_fma_f32 v105, -v189, v93, v105
	v_fma_f32 v106, -v190, v94, v106
	v_fma_f32 v107, -v191, v95, v107
	v_fma_f32 v104, -v192, v96, v104
	v_fma_f32 v105, -v193, v97, v105
	v_fma_f32 v106, -v194, v98, v106
	v_fma_f32 v107, -v195, v99, v107
	v_fma_f32 v104, -v196, v100, v104
	v_fma_f32 v105, -v197, v101, v105
	v_fma_f32 v106, -v198, v102, v106
	v_add_f32_e32 v104, v104, v105
	v_add_f32_e32 v106, v106, v107
	v_add_f32_e32 v103, v104, v106
	ds_write_b32 v1, v72 offset:0
	ds_write_b32 v1, v73 offset:128
	ds_write_b32 v1, v74 offset:256
	ds_write_b32 v1, v75 offset:384
	ds_write_b32 v1, v76 offset:512
	ds_write_b32 v1, v77 offset:640
	ds_write_b32 v1, v78 offset:768
	ds_write_b32 v1, v79 offset:896
	ds_write_b32 v1, v80 offset:1024
	ds_write_b32 v1, v81 offset:1152
	ds_write_b32 v1, v82 offset:1280
	ds_write_b32 v1, v83 offset:1408
	ds_write_b32 v1, v84 offset:1536
	ds_write_b32 v1, v85 offset:1664
	ds_write_b32 v1, v86 offset:1792
	ds_write_b32 v1, v87 offset:1920
	ds_write_b32 v1, v88 offset:2048
	ds_write_b32 v1, v89 offset:2176
	ds_write_b32 v1, v90 offset:2304
	ds_write_b32 v1, v91 offset:2432
	ds_write_b32 v1, v92 offset:2560
	ds_write_b32 v1, v93 offset:2688
	ds_write_b32 v1, v94 offset:2816
	ds_write_b32 v1, v95 offset:2944
	ds_write_b32 v1, v96 offset:3072
	ds_write_b32 v1, v97 offset:3200
	ds_write_b32 v1, v98 offset:3328
	ds_write_b32 v1, v99 offset:3456
	ds_write_b32 v1, v100 offset:3584
	ds_write_b32 v1, v101 offset:3712
	ds_write_b32 v1, v102 offset:3840
	ds_write_b32 v1, v103 offset:3968
.Lg4_s1done:
	s_waitcnt lgkmcnt(0)
	s_barrier
	s_lshr_b32 s1, s10, 2
	s_and_b32 s11, s10, 3
	v_lshrrev_b32_e32 v4, 5, v21
	v_and_b32_e32 v108, 31, v21
	s_mul_i32 s12, s1, 0x3000
	v_lshl_add_u32 v4, s11, 1, v4
	s_mul_i32 s13, s1, 0x4800
	s_add_i32 s12, s12, 0x1b000
	v_lshlrev_b32_e32 v5, 2, v108
	v_mul_u32_u24_e32 v6, 0x440, v4
	v_lshlrev_b32_e32 v7, 9, v4
	v_add3_u32 v8, v61, v5, s12
	s_add_i32 s24, s13, 0x2200
	v_add3_u32 v9, v61, v6, s24
	v_add_u32_e32 v10, v8, v7
	v_add3_u32 v11, v61, v7, s12
	ds_read_b32 v200, v8 offset:0
	ds_read_b32 v201, v8 offset:128
	ds_read_b32 v202, v8 offset:256
	ds_read_b32 v203, v8 offset:384
	ds_read_b32 v204, v8 offset:512
	ds_read_b32 v205, v8 offset:640
	ds_read_b32 v206, v8 offset:768
	ds_read_b32 v207, v8 offset:896
	ds_read_b32 v208, v8 offset:1024
	ds_read_b32 v209, v8 offset:1152
	ds_read_b32 v210, v8 offset:1280
	ds_read_b32 v211, v8 offset:1408
	ds_read_b32 v212, v8 offset:1536
	ds_read_b32 v213, v8 offset:1664
	ds_read_b32 v214, v8 offset:1792
	ds_read_b32 v215, v8 offset:1920
	ds_read_b32 v216, v8 offset:2048
	ds_read_b32 v217, v8 offset:2176
	ds_read_b32 v218, v8 offset:2304
	ds_read_b32 v219, v8 offset:2432
	ds_read_b32 v220, v8 offset:2560
	ds_read_b32 v221, v8 offset:2688
	ds_read_b32 v222, v8 offset:2816
	ds_read_b32 v223, v8 offset:2944
	ds_read_b32 v224, v8 offset:3072
	ds_read_b32 v225, v8 offset:3200
	ds_read_b32 v226, v8 offset:3328
	ds_read_b32 v227, v8 offset:3456
	ds_read_b32 v228, v8 offset:3584
	ds_read_b32 v229, v8 offset:3712
	ds_read_b32 v230, v8 offset:3840
	ds_read_b32 v231, v8 offset:3968
	ds_read_b128 v[136:139], v9 offset:0
	ds_read_b128 v[140:143], v9 offset:16
	ds_read_b128 v[144:147], v9 offset:32
	ds_read_b128 v[148:151], v9 offset:48
	ds_read_b128 v[152:155], v9 offset:64
	ds_read_b128 v[156:159], v9 offset:80
	ds_read_b128 v[160:163], v9 offset:96
	ds_read_b128 v[164:167], v9 offset:112
	s_waitcnt lgkmcnt(0)
	ds_read_b128 v[168:171], v9 offset:272
	ds_read_b128 v[172:175], v9 offset:288
	ds_read_b128 v[176:179], v9 offset:304
	ds_read_b128 v[180:183], v9 offset:320
	ds_read_b128 v[184:187], v9 offset:336
	ds_read_b128 v[188:191], v9 offset:352
	ds_read_b128 v[192:195], v9 offset:368
	ds_read_b128 v[196:199], v9 offset:384
	v_mul_f32_e32 v104, v136, v200
	v_mul_f32_e32 v105, v137, v201
	v_fmac_f32_e32 v104, v138, v202
	v_fmac_f32_e32 v105, v139, v203
	v_fmac_f32_e32 v104, v140, v204
	v_fmac_f32_e32 v105, v141, v205
	v_fmac_f32_e32 v104, v142, v206
	v_fmac_f32_e32 v105, v143, v207
	v_fmac_f32_e32 v104, v144, v208
	v_fmac_f32_e32 v105, v145, v209
	v_fmac_f32_e32 v104, v146, v210
	v_fmac_f32_e32 v105, v147, v211
	v_fmac_f32_e32 v104, v148, v212
	v_fmac_f32_e32 v105, v149, v213
	v_fmac_f32_e32 v104, v150, v214
	v_fmac_f32_e32 v105, v151, v215
	v_fmac_f32_e32 v104, v152, v216
	v_fmac_f32_e32 v105, v153, v217
	v_fmac_f32_e32 v104, v154, v218
	v_fmac_f32_e32 v105, v155, v219
	v_fmac_f32_e32 v104, v156, v220
	v_fmac_f32_e32 v105, v157, v221
	v_fmac_f32_e32 v104, v158, v222
	v_fmac_f32_e32 v105, v159, v223
	v_fmac_f32_e32 v104, v160, v224
	v_fmac_f32_e32 v105, v161, v225
	v_fmac_f32_e32 v104, v162, v226
	v_fmac_f32_e32 v105, v163, v227
	v_fmac_f32_e32 v104, v164, v228
	v_fmac_f32_e32 v105, v165, v229
	v_fmac_f32_e32 v104, v166, v230
	v_fmac_f32_e32 v105, v167, v231
	v_add_f32_e32 v232, v104, v105
	s_waitcnt lgkmcnt(0)
	ds_read_b128 v[136:139], v9 offset:544
	ds_read_b128 v[140:143], v9 offset:560
	ds_read_b128 v[144:147], v9 offset:576
	ds_read_b128 v[148:151], v9 offset:592
	ds_read_b128 v[152:155], v9 offset:608
	ds_read_b128 v[156:159], v9 offset:624
	ds_read_b128 v[160:163], v9 offset:640
	ds_read_b128 v[164:167], v9 offset:656
	v_mul_f32_e32 v104, v168, v200
	v_mul_f32_e32 v105, v169, v201
	v_fmac_f32_e32 v104, v170, v202
	v_fmac_f32_e32 v105, v171, v203
	v_fmac_f32_e32 v104, v172, v204
	v_fmac_f32_e32 v105, v173, v205
	v_fmac_f32_e32 v104, v174, v206
	v_fmac_f32_e32 v105, v175, v207
	v_fmac_f32_e32 v104, v176, v208
	v_fmac_f32_e32 v105, v177, v209
	v_fmac_f32_e32 v104, v178, v210
	v_fmac_f32_e32 v105, v179, v211
	v_fmac_f32_e32 v104, v180, v212
	v_fmac_f32_e32 v105, v181, v213
	v_fmac_f32_e32 v104, v182, v214
	v_fmac_f32_e32 v105, v183, v215
	v_fmac_f32_e32 v104, v184, v216
	v_fmac_f32_e32 v105, v185, v217
	v_fmac_f32_e32 v104, v186, v218
	v_fmac_f32_e32 v105, v187, v219
	v_fmac_f32_e32 v104, v188, v220
	v_fmac_f32_e32 v105, v189, v221
	v_fmac_f32_e32 v104, v190, v222
	v_fmac_f32_e32 v105, v191, v223
	v_fmac_f32_e32 v104, v192, v224
	v_fmac_f32_e32 v105, v193, v225
	v_fmac_f32_e32 v104, v194, v226
	v_fmac_f32_e32 v105, v195, v227
	v_fmac_f32_e32 v104, v196, v228
	v_fmac_f32_e32 v105, v197, v229
	v_fmac_f32_e32 v104, v198, v230
	v_fmac_f32_e32 v105, v199, v231
	v_add_f32_e32 v233, v104, v105
	s_waitcnt lgkmcnt(0)
	ds_read_b128 v[168:171], v9 offset:816
	ds_read_b128 v[172:175], v9 offset:832
	ds_read_b128 v[176:179], v9 offset:848
	ds_read_b128 v[180:183], v9 offset:864
	ds_read_b128 v[184:187], v9 offset:880
	ds_read_b128 v[188:191], v9 offset:896
	ds_read_b128 v[192:195], v9 offset:912
	ds_read_b128 v[196:199], v9 offset:928
	v_mul_f32_e32 v104, v136, v200
	v_mul_f32_e32 v105, v137, v201
	v_fmac_f32_e32 v104, v138, v202
	v_fmac_f32_e32 v105, v139, v203
	v_fmac_f32_e32 v104, v140, v204
	v_fmac_f32_e32 v105, v141, v205
	v_fmac_f32_e32 v104, v142, v206
	v_fmac_f32_e32 v105, v143, v207
	v_fmac_f32_e32 v104, v144, v208
	v_fmac_f32_e32 v105, v145, v209
	v_fmac_f32_e32 v104, v146, v210
	v_fmac_f32_e32 v105, v147, v211
	v_fmac_f32_e32 v104, v148, v212
	v_fmac_f32_e32 v105, v149, v213
	v_fmac_f32_e32 v104, v150, v214
	v_fmac_f32_e32 v105, v151, v215
	v_fmac_f32_e32 v104, v152, v216
	v_fmac_f32_e32 v105, v153, v217
	v_fmac_f32_e32 v104, v154, v218
	v_fmac_f32_e32 v105, v155, v219
	v_fmac_f32_e32 v104, v156, v220
	v_fmac_f32_e32 v105, v157, v221
	v_fmac_f32_e32 v104, v158, v222
	v_fmac_f32_e32 v105, v159, v223
	v_fmac_f32_e32 v104, v160, v224
	v_fmac_f32_e32 v105, v161, v225
	v_fmac_f32_e32 v104, v162, v226
	v_fmac_f32_e32 v105, v163, v227
	v_fmac_f32_e32 v104, v164, v228
	v_fmac_f32_e32 v105, v165, v229
	v_fmac_f32_e32 v104, v166, v230
	v_fmac_f32_e32 v105, v167, v231
	v_add_f32_e32 v234, v104, v105
	s_waitcnt lgkmcnt(0)
	v_mul_f32_e32 v104, v168, v200
	v_mul_f32_e32 v105, v169, v201
	v_fmac_f32_e32 v104, v170, v202
	v_fmac_f32_e32 v105, v171, v203
	v_fmac_f32_e32 v104, v172, v204
	v_fmac_f32_e32 v105, v173, v205
	v_fmac_f32_e32 v104, v174, v206
	v_fmac_f32_e32 v105, v175, v207
	v_fmac_f32_e32 v104, v176, v208
	v_fmac_f32_e32 v105, v177, v209
	v_fmac_f32_e32 v104, v178, v210
	v_fmac_f32_e32 v105, v179, v211
	v_fmac_f32_e32 v104, v180, v212
	v_fmac_f32_e32 v105, v181, v213
	v_fmac_f32_e32 v104, v182, v214
	v_fmac_f32_e32 v105, v183, v215
	v_fmac_f32_e32 v104, v184, v216
	v_fmac_f32_e32 v105, v185, v217
	v_fmac_f32_e32 v104, v186, v218
	v_fmac_f32_e32 v105, v187, v219
	v_fmac_f32_e32 v104, v188, v220
	v_fmac_f32_e32 v105, v189, v221
	v_fmac_f32_e32 v104, v190, v222
	v_fmac_f32_e32 v105, v191, v223
	v_fmac_f32_e32 v104, v192, v224
	v_fmac_f32_e32 v105, v193, v225
	v_fmac_f32_e32 v104, v194, v226
	v_fmac_f32_e32 v105, v195, v227
	v_fmac_f32_e32 v104, v196, v228
	v_fmac_f32_e32 v105, v197, v229
	v_fmac_f32_e32 v104, v198, v230
	v_fmac_f32_e32 v105, v199, v231
	v_add_f32_e32 v235, v104, v105
	ds_write_b32 v10, v232 offset:8192
	ds_write_b32 v10, v233 offset:8320
	ds_write_b32 v10, v234 offset:8448
	ds_write_b32 v10, v235 offset:8576
	s_waitcnt lgkmcnt(0)
	s_barrier
	ds_read_b32 v200, v8 offset:8192
	ds_read_b32 v201, v8 offset:8320
	ds_read_b32 v202, v8 offset:8448
	ds_read_b32 v203, v8 offset:8576
	ds_read_b32 v204, v8 offset:8704
	ds_read_b32 v205, v8 offset:8832
	ds_read_b32 v206, v8 offset:8960
	ds_read_b32 v207, v8 offset:9088
	ds_read_b32 v208, v8 offset:9216
	ds_read_b32 v209, v8 offset:9344
	ds_read_b32 v210, v8 offset:9472
	ds_read_b32 v211, v8 offset:9600
	ds_read_b32 v212, v8 offset:9728
	ds_read_b32 v213, v8 offset:9856
	ds_read_b32 v214, v8 offset:9984
	ds_read_b32 v215, v8 offset:10112
	ds_read_b32 v216, v8 offset:10240
	ds_read_b32 v217, v8 offset:10368
	ds_read_b32 v218, v8 offset:10496
	ds_read_b32 v219, v8 offset:10624
	ds_read_b32 v220, v8 offset:10752
	ds_read_b32 v221, v8 offset:10880
	ds_read_b32 v222, v8 offset:11008
	ds_read_b32 v223, v8 offset:11136
	ds_read_b32 v224, v8 offset:11264
	ds_read_b32 v225, v8 offset:11392
	ds_read_b32 v226, v8 offset:11520
	ds_read_b32 v227, v8 offset:11648
	ds_read_b32 v228, v8 offset:11776
	ds_read_b32 v229, v8 offset:11904
	ds_read_b32 v230, v8 offset:12032
	ds_read_b32 v231, v8 offset:12160
	ds_read_b128 v[136:139], v11 offset:4096
	ds_read_b128 v[140:143], v11 offset:4112
	ds_read_b128 v[144:147], v11 offset:4128
	ds_read_b128 v[148:151], v11 offset:4144
	ds_read_b128 v[152:155], v11 offset:4160
	ds_read_b128 v[156:159], v11 offset:4176
	ds_read_b128 v[160:163], v11 offset:4192
	ds_read_b128 v[164:167], v11 offset:4208
	s_waitcnt lgkmcnt(0)
	ds_read_b128 v[168:171], v11 offset:4224
	ds_read_b128 v[172:175], v11 offset:4240
	ds_read_b128 v[176:179], v11 offset:4256
	ds_read_b128 v[180:183], v11 offset:4272
	ds_read_b128 v[184:187], v11 offset:4288
	ds_read_b128 v[188:191], v11 offset:4304
	ds_read_b128 v[192:195], v11 offset:4320
	ds_read_b128 v[196:199], v11 offset:4336
	v_mul_f32_e32 v104, v136, v200
	v_mul_f32_e32 v105, v137, v201
	v_fmac_f32_e32 v104, v138, v202
	v_fmac_f32_e32 v105, v139, v203
	v_fmac_f32_e32 v104, v140, v204
	v_fmac_f32_e32 v105, v141, v205
	v_fmac_f32_e32 v104, v142, v206
	v_fmac_f32_e32 v105, v143, v207
	v_fmac_f32_e32 v104, v144, v208
	v_fmac_f32_e32 v105, v145, v209
	v_fmac_f32_e32 v104, v146, v210
	v_fmac_f32_e32 v105, v147, v211
	v_fmac_f32_e32 v104, v148, v212
	v_fmac_f32_e32 v105, v149, v213
	v_fmac_f32_e32 v104, v150, v214
	v_fmac_f32_e32 v105, v151, v215
	v_fmac_f32_e32 v104, v152, v216
	v_fmac_f32_e32 v105, v153, v217
	v_fmac_f32_e32 v104, v154, v218
	v_fmac_f32_e32 v105, v155, v219
	v_fmac_f32_e32 v104, v156, v220
	v_fmac_f32_e32 v105, v157, v221
	v_fmac_f32_e32 v104, v158, v222
	v_fmac_f32_e32 v105, v159, v223
	v_fmac_f32_e32 v104, v160, v224
	v_fmac_f32_e32 v105, v161, v225
	v_fmac_f32_e32 v104, v162, v226
	v_fmac_f32_e32 v105, v163, v227
	v_fmac_f32_e32 v104, v164, v228
	v_fmac_f32_e32 v105, v165, v229
	v_fmac_f32_e32 v104, v166, v230
	v_fmac_f32_e32 v105, v167, v231
	v_add_f32_e32 v232, v104, v105
	s_waitcnt lgkmcnt(0)
	ds_read_b128 v[136:139], v11 offset:4352
	ds_read_b128 v[140:143], v11 offset:4368
	ds_read_b128 v[144:147], v11 offset:4384
	ds_read_b128 v[148:151], v11 offset:4400
	ds_read_b128 v[152:155], v11 offset:4416
	ds_read_b128 v[156:159], v11 offset:4432
	ds_read_b128 v[160:163], v11 offset:4448
	ds_read_b128 v[164:167], v11 offset:4464
	v_mul_f32_e32 v104, v168, v200
	v_mul_f32_e32 v105, v169, v201
	v_fmac_f32_e32 v104, v170, v202
	v_fmac_f32_e32 v105, v171, v203
	v_fmac_f32_e32 v104, v172, v204
	v_fmac_f32_e32 v105, v173, v205
	v_fmac_f32_e32 v104, v174, v206
	v_fmac_f32_e32 v105, v175, v207
	v_fmac_f32_e32 v104, v176, v208
	v_fmac_f32_e32 v105, v177, v209
	v_fmac_f32_e32 v104, v178, v210
	v_fmac_f32_e32 v105, v179, v211
	v_fmac_f32_e32 v104, v180, v212
	v_fmac_f32_e32 v105, v181, v213
	v_fmac_f32_e32 v104, v182, v214
	v_fmac_f32_e32 v105, v183, v215
	v_fmac_f32_e32 v104, v184, v216
	v_fmac_f32_e32 v105, v185, v217
	v_fmac_f32_e32 v104, v186, v218
	v_fmac_f32_e32 v105, v187, v219
	v_fmac_f32_e32 v104, v188, v220
	v_fmac_f32_e32 v105, v189, v221
	v_fmac_f32_e32 v104, v190, v222
	v_fmac_f32_e32 v105, v191, v223
	v_fmac_f32_e32 v104, v192, v224
	v_fmac_f32_e32 v105, v193, v225
	v_fmac_f32_e32 v104, v194, v226
	v_fmac_f32_e32 v105, v195, v227
	v_fmac_f32_e32 v104, v196, v228
	v_fmac_f32_e32 v105, v197, v229
	v_fmac_f32_e32 v104, v198, v230
	v_fmac_f32_e32 v105, v199, v231
	v_add_f32_e32 v233, v104, v105
	s_waitcnt lgkmcnt(0)
	ds_read_b128 v[168:171], v11 offset:4480
	ds_read_b128 v[172:175], v11 offset:4496
	ds_read_b128 v[176:179], v11 offset:4512
	ds_read_b128 v[180:183], v11 offset:4528
	ds_read_b128 v[184:187], v11 offset:4544
	ds_read_b128 v[188:191], v11 offset:4560
	ds_read_b128 v[192:195], v11 offset:4576
	ds_read_b128 v[196:199], v11 offset:4592
	v_mul_f32_e32 v104, v136, v200
	v_mul_f32_e32 v105, v137, v201
	v_fmac_f32_e32 v104, v138, v202
	v_fmac_f32_e32 v105, v139, v203
	v_fmac_f32_e32 v104, v140, v204
	v_fmac_f32_e32 v105, v141, v205
	v_fmac_f32_e32 v104, v142, v206
	v_fmac_f32_e32 v105, v143, v207
	v_fmac_f32_e32 v104, v144, v208
	v_fmac_f32_e32 v105, v145, v209
	v_fmac_f32_e32 v104, v146, v210
	v_fmac_f32_e32 v105, v147, v211
	v_fmac_f32_e32 v104, v148, v212
	v_fmac_f32_e32 v105, v149, v213
	v_fmac_f32_e32 v104, v150, v214
	v_fmac_f32_e32 v105, v151, v215
	v_fmac_f32_e32 v104, v152, v216
	v_fmac_f32_e32 v105, v153, v217
	v_fmac_f32_e32 v104, v154, v218
	v_fmac_f32_e32 v105, v155, v219
	v_fmac_f32_e32 v104, v156, v220
	v_fmac_f32_e32 v105, v157, v221
	v_fmac_f32_e32 v104, v158, v222
	v_fmac_f32_e32 v105, v159, v223
	v_fmac_f32_e32 v104, v160, v224
	v_fmac_f32_e32 v105, v161, v225
	v_fmac_f32_e32 v104, v162, v226
	v_fmac_f32_e32 v105, v163, v227
	v_fmac_f32_e32 v104, v164, v228
	v_fmac_f32_e32 v105, v165, v229
	v_fmac_f32_e32 v104, v166, v230
	v_fmac_f32_e32 v105, v167, v231
	v_add_f32_e32 v234, v104, v105
	s_waitcnt lgkmcnt(0)
	v_mul_f32_e32 v104, v168, v200
	v_mul_f32_e32 v105, v169, v201
	v_fmac_f32_e32 v104, v170, v202
	v_fmac_f32_e32 v105, v171, v203
	v_fmac_f32_e32 v104, v172, v204
	v_fmac_f32_e32 v105, v173, v205
	v_fmac_f32_e32 v104, v174, v206
	v_fmac_f32_e32 v105, v175, v207
	v_fmac_f32_e32 v104, v176, v208
	v_fmac_f32_e32 v105, v177, v209
	v_fmac_f32_e32 v104, v178, v210
	v_fmac_f32_e32 v105, v179, v211
	v_fmac_f32_e32 v104, v180, v212
	v_fmac_f32_e32 v105, v181, v213
	v_fmac_f32_e32 v104, v182, v214
	v_fmac_f32_e32 v105, v183, v215
	v_fmac_f32_e32 v104, v184, v216
	v_fmac_f32_e32 v105, v185, v217
	v_fmac_f32_e32 v104, v186, v218
	v_fmac_f32_e32 v105, v187, v219
	v_fmac_f32_e32 v104, v188, v220
	v_fmac_f32_e32 v105, v189, v221
	v_fmac_f32_e32 v104, v190, v222
	v_fmac_f32_e32 v105, v191, v223
	v_fmac_f32_e32 v104, v192, v224
	v_fmac_f32_e32 v105, v193, v225
	v_fmac_f32_e32 v104, v194, v226
	v_fmac_f32_e32 v105, v195, v227
	v_fmac_f32_e32 v104, v196, v228
	v_fmac_f32_e32 v105, v197, v229
	v_fmac_f32_e32 v104, v198, v230
	v_fmac_f32_e32 v105, v199, v231
	v_add_f32_e32 v235, v104, v105
	s_lshl_b32 s24, s1, 8
	s_add_i32 s24, s24, 0x23200
	v_add3_u32 v12, v61, v5, s24
	ds_read_b32 v13, v12
	ds_read_b32 v14, v12 offset:512
	v_mul_u32_u24_e32 v15, 0x240, v4
	s_add_i32 s24, s13, 0x1200
	v_lshl_add_u32 v15, v108, 1, v15
	v_add3_u32 v15, v61, v15, s24
	s_waitcnt lgkmcnt(0)
	v_mul_f32_e32 v13, 0x3fb8aa3b, v13
	v_exp_f32_e32 v13, v13
	s_nop 0
	v_mul_f32_e32 v13, v14, v13
	v_mul_f32_e64 v16, -v232, v13
	v_mul_f32_e64 v17, -v232, v14
	v_cvt_pk_bf16_f32 v16, v16, v16
	v_cvt_pk_bf16_f32 v17, v17, v17
	ds_write_b16 v15, v16 offset:0
	ds_write_b16 v15, v17 offset:9216
	v_mul_f32_e64 v16, -v233, v13
	v_mul_f32_e64 v17, -v233, v14
	v_cvt_pk_bf16_f32 v16, v16, v16
	v_cvt_pk_bf16_f32 v17, v17, v17
	ds_write_b16 v15, v16 offset:144
	ds_write_b16 v15, v17 offset:9360
	v_mul_f32_e64 v16, -v234, v13
	v_mul_f32_e64 v17, -v234, v14
	v_cvt_pk_bf16_f32 v16, v16, v16
	v_cvt_pk_bf16_f32 v17, v17, v17
	ds_write_b16 v15, v16 offset:288
	ds_write_b16 v15, v17 offset:9504
	v_mul_f32_e64 v16, -v235, v13
	v_mul_f32_e64 v17, -v235, v14
	v_cvt_pk_bf16_f32 v16, v16, v16
	v_cvt_pk_bf16_f32 v17, v17, v17
	ds_write_b16 v15, v16 offset:432
	ds_write_b16 v15, v17 offset:9648
	s_cmp_gt_u32 s10, 1
	s_cbranch_scc1 .Lg4_done
	s_lshl_b32 s24, s10, 8
	v_lshlrev_b32_e32 v5, 2, v21
	s_add_i32 s24, s24, 0x23200
	v_lshrrev_b32_e32 v4, 5, v21
	v_add3_u32 v12, v61, v5, s24
	ds_read_b32 v13, v12
	ds_read_b32 v14, v12 offset:512
	v_mul_u32_u24_e32 v6, 0x1200, v4
	s_mul_i32 s24, s10, 0x4800
	v_lshl_add_u32 v6, v21, 1, v6
	v_add3_u32 v15, v61, v6, s24
	s_waitcnt lgkmcnt(0)
	v_mul_f32_e32 v13, 0x3fb8aa3b, v13
	v_exp_f32_e32 v13, v13
	s_nop 0
	v_mul_f32_e32 v13, v14, v13
	v_mul_f32_e32 v16, v72, v13
	v_mul_f32_e32 v17, v72, v14
	v_cvt_pk_bf16_f32 v16, v16, v16
	v_cvt_pk_bf16_f32 v17, v17, v17
	ds_write_b16 v15, v16 offset:0
	ds_write_b16 v15, v17 offset:9216
	v_mul_f32_e32 v16, v73, v13
	v_mul_f32_e32 v17, v73, v14
	v_cvt_pk_bf16_f32 v16, v16, v16
	v_cvt_pk_bf16_f32 v17, v17, v17
	ds_write_b16 v15, v16 offset:144
	ds_write_b16 v15, v17 offset:9360
	v_mul_f32_e32 v16, v74, v13
	v_mul_f32_e32 v17, v74, v14
	v_cvt_pk_bf16_f32 v16, v16, v16
	v_cvt_pk_bf16_f32 v17, v17, v17
	ds_write_b16 v15, v16 offset:288
	ds_write_b16 v15, v17 offset:9504
	v_mul_f32_e32 v16, v75, v13
	v_mul_f32_e32 v17, v75, v14
	v_cvt_pk_bf16_f32 v16, v16, v16
	v_cvt_pk_bf16_f32 v17, v17, v17
	ds_write_b16 v15, v16 offset:432
	ds_write_b16 v15, v17 offset:9648
	v_mul_f32_e32 v16, v76, v13
	v_mul_f32_e32 v17, v76, v14
	v_cvt_pk_bf16_f32 v16, v16, v16
	v_cvt_pk_bf16_f32 v17, v17, v17
	ds_write_b16 v15, v16 offset:576
	ds_write_b16 v15, v17 offset:9792
	v_mul_f32_e32 v16, v77, v13
	v_mul_f32_e32 v17, v77, v14
	v_cvt_pk_bf16_f32 v16, v16, v16
	v_cvt_pk_bf16_f32 v17, v17, v17
	ds_write_b16 v15, v16 offset:720
	ds_write_b16 v15, v17 offset:9936
	v_mul_f32_e32 v16, v78, v13
	v_mul_f32_e32 v17, v78, v14
	v_cvt_pk_bf16_f32 v16, v16, v16
	v_cvt_pk_bf16_f32 v17, v17, v17
	ds_write_b16 v15, v16 offset:864
	ds_write_b16 v15, v17 offset:10080
	v_mul_f32_e32 v16, v79, v13
	v_mul_f32_e32 v17, v79, v14
	v_cvt_pk_bf16_f32 v16, v16, v16
	v_cvt_pk_bf16_f32 v17, v17, v17
	ds_write_b16 v15, v16 offset:1008
	ds_write_b16 v15, v17 offset:10224
	v_mul_f32_e32 v16, v80, v13
	v_mul_f32_e32 v17, v80, v14
	v_cvt_pk_bf16_f32 v16, v16, v16
	v_cvt_pk_bf16_f32 v17, v17, v17
	ds_write_b16 v15, v16 offset:1152
	ds_write_b16 v15, v17 offset:10368
	v_mul_f32_e32 v16, v81, v13
	v_mul_f32_e32 v17, v81, v14
	v_cvt_pk_bf16_f32 v16, v16, v16
	v_cvt_pk_bf16_f32 v17, v17, v17
	ds_write_b16 v15, v16 offset:1296
	ds_write_b16 v15, v17 offset:10512
	v_mul_f32_e32 v16, v82, v13
	v_mul_f32_e32 v17, v82, v14
	v_cvt_pk_bf16_f32 v16, v16, v16
	v_cvt_pk_bf16_f32 v17, v17, v17
	ds_write_b16 v15, v16 offset:1440
	ds_write_b16 v15, v17 offset:10656
	v_mul_f32_e32 v16, v83, v13
	v_mul_f32_e32 v17, v83, v14
	v_cvt_pk_bf16_f32 v16, v16, v16
	v_cvt_pk_bf16_f32 v17, v17, v17
	ds_write_b16 v15, v16 offset:1584
	ds_write_b16 v15, v17 offset:10800
	v_mul_f32_e32 v16, v84, v13
	v_mul_f32_e32 v17, v84, v14
	v_cvt_pk_bf16_f32 v16, v16, v16
	v_cvt_pk_bf16_f32 v17, v17, v17
	ds_write_b16 v15, v16 offset:1728
	ds_write_b16 v15, v17 offset:10944
	v_mul_f32_e32 v16, v85, v13
	v_mul_f32_e32 v17, v85, v14
	v_cvt_pk_bf16_f32 v16, v16, v16
	v_cvt_pk_bf16_f32 v17, v17, v17
	ds_write_b16 v15, v16 offset:1872
	ds_write_b16 v15, v17 offset:11088
	v_mul_f32_e32 v16, v86, v13
	v_mul_f32_e32 v17, v86, v14
	v_cvt_pk_bf16_f32 v16, v16, v16
	v_cvt_pk_bf16_f32 v17, v17, v17
	ds_write_b16 v15, v16 offset:2016
	ds_write_b16 v15, v17 offset:11232
	v_mul_f32_e32 v16, v87, v13
	v_mul_f32_e32 v17, v87, v14
	v_cvt_pk_bf16_f32 v16, v16, v16
	v_cvt_pk_bf16_f32 v17, v17, v17
	ds_write_b16 v15, v16 offset:2160
	ds_write_b16 v15, v17 offset:11376
	v_mul_f32_e32 v16, v88, v13
	v_mul_f32_e32 v17, v88, v14
	v_cvt_pk_bf16_f32 v16, v16, v16
	v_cvt_pk_bf16_f32 v17, v17, v17
	ds_write_b16 v15, v16 offset:2304
	ds_write_b16 v15, v17 offset:11520
	v_mul_f32_e32 v16, v89, v13
	v_mul_f32_e32 v17, v89, v14
	v_cvt_pk_bf16_f32 v16, v16, v16
	v_cvt_pk_bf16_f32 v17, v17, v17
	ds_write_b16 v15, v16 offset:2448
	ds_write_b16 v15, v17 offset:11664
	v_mul_f32_e32 v16, v90, v13
	v_mul_f32_e32 v17, v90, v14
	v_cvt_pk_bf16_f32 v16, v16, v16
	v_cvt_pk_bf16_f32 v17, v17, v17
	ds_write_b16 v15, v16 offset:2592
	ds_write_b16 v15, v17 offset:11808
	v_mul_f32_e32 v16, v91, v13
	v_mul_f32_e32 v17, v91, v14
	v_cvt_pk_bf16_f32 v16, v16, v16
	v_cvt_pk_bf16_f32 v17, v17, v17
	ds_write_b16 v15, v16 offset:2736
	ds_write_b16 v15, v17 offset:11952
	v_mul_f32_e32 v16, v92, v13
	v_mul_f32_e32 v17, v92, v14
	v_cvt_pk_bf16_f32 v16, v16, v16
	v_cvt_pk_bf16_f32 v17, v17, v17
	ds_write_b16 v15, v16 offset:2880
	ds_write_b16 v15, v17 offset:12096
	v_mul_f32_e32 v16, v93, v13
	v_mul_f32_e32 v17, v93, v14
	v_cvt_pk_bf16_f32 v16, v16, v16
	v_cvt_pk_bf16_f32 v17, v17, v17
	ds_write_b16 v15, v16 offset:3024
	ds_write_b16 v15, v17 offset:12240
	v_mul_f32_e32 v16, v94, v13
	v_mul_f32_e32 v17, v94, v14
	v_cvt_pk_bf16_f32 v16, v16, v16
	v_cvt_pk_bf16_f32 v17, v17, v17
	ds_write_b16 v15, v16 offset:3168
	ds_write_b16 v15, v17 offset:12384
	v_mul_f32_e32 v16, v95, v13
	v_mul_f32_e32 v17, v95, v14
	v_cvt_pk_bf16_f32 v16, v16, v16
	v_cvt_pk_bf16_f32 v17, v17, v17
	ds_write_b16 v15, v16 offset:3312
	ds_write_b16 v15, v17 offset:12528
	v_mul_f32_e32 v16, v96, v13
	v_mul_f32_e32 v17, v96, v14
	v_cvt_pk_bf16_f32 v16, v16, v16
	v_cvt_pk_bf16_f32 v17, v17, v17
	ds_write_b16 v15, v16 offset:3456
	ds_write_b16 v15, v17 offset:12672
	v_mul_f32_e32 v16, v97, v13
	v_mul_f32_e32 v17, v97, v14
	v_cvt_pk_bf16_f32 v16, v16, v16
	v_cvt_pk_bf16_f32 v17, v17, v17
	ds_write_b16 v15, v16 offset:3600
	ds_write_b16 v15, v17 offset:12816
	v_mul_f32_e32 v16, v98, v13
	v_mul_f32_e32 v17, v98, v14
	v_cvt_pk_bf16_f32 v16, v16, v16
	v_cvt_pk_bf16_f32 v17, v17, v17
	ds_write_b16 v15, v16 offset:3744
	ds_write_b16 v15, v17 offset:12960
	v_mul_f32_e32 v16, v99, v13
	v_mul_f32_e32 v17, v99, v14
	v_cvt_pk_bf16_f32 v16, v16, v16
	v_cvt_pk_bf16_f32 v17, v17, v17
	ds_write_b16 v15, v16 offset:3888
	ds_write_b16 v15, v17 offset:13104
	v_mul_f32_e32 v16, v100, v13
	v_mul_f32_e32 v17, v100, v14
	v_cvt_pk_bf16_f32 v16, v16, v16
	v_cvt_pk_bf16_f32 v17, v17, v17
	ds_write_b16 v15, v16 offset:4032
	ds_write_b16 v15, v17 offset:13248
	v_mul_f32_e32 v16, v101, v13
	v_mul_f32_e32 v17, v101, v14
	v_cvt_pk_bf16_f32 v16, v16, v16
	v_cvt_pk_bf16_f32 v17, v17, v17
	ds_write_b16 v15, v16 offset:4176
	ds_write_b16 v15, v17 offset:13392
	v_mul_f32_e32 v16, v102, v13
	v_mul_f32_e32 v17, v102, v14
	v_cvt_pk_bf16_f32 v16, v16, v16
	v_cvt_pk_bf16_f32 v17, v17, v17
	ds_write_b16 v15, v16 offset:4320
	ds_write_b16 v15, v17 offset:13536
	v_mul_f32_e32 v16, v103, v13
	v_mul_f32_e32 v17, v103, v14
	v_cvt_pk_bf16_f32 v16, v16, v16
	v_cvt_pk_bf16_f32 v17, v17, v17
	ds_write_b16 v15, v16 offset:4464
	ds_write_b16 v15, v17 offset:13680
	v_cmp_lt_u32_e32 vcc, 31, v21
	v_subrev_u32_e32 v18, 0x1200, v15
	v_mov_b32_e32 v19, 0
	s_and_saveexec_b64 s[12:13], vcc
	ds_write_b16 v18, v19 offset:0
	ds_write_b16 v18, v19 offset:9216
	ds_write_b16 v18, v19 offset:144
	ds_write_b16 v18, v19 offset:9360
	ds_write_b16 v18, v19 offset:288
	ds_write_b16 v18, v19 offset:9504
	ds_write_b16 v18, v19 offset:432
	ds_write_b16 v18, v19 offset:9648
	ds_write_b16 v18, v19 offset:576
	ds_write_b16 v18, v19 offset:9792
	ds_write_b16 v18, v19 offset:720
	ds_write_b16 v18, v19 offset:9936
	ds_write_b16 v18, v19 offset:864
	ds_write_b16 v18, v19 offset:10080
	ds_write_b16 v18, v19 offset:1008
	ds_write_b16 v18, v19 offset:10224
	ds_write_b16 v18, v19 offset:1152
	ds_write_b16 v18, v19 offset:10368
	ds_write_b16 v18, v19 offset:1296
	ds_write_b16 v18, v19 offset:10512
	ds_write_b16 v18, v19 offset:1440
	ds_write_b16 v18, v19 offset:10656
	ds_write_b16 v18, v19 offset:1584
	ds_write_b16 v18, v19 offset:10800
	ds_write_b16 v18, v19 offset:1728
	ds_write_b16 v18, v19 offset:10944
	ds_write_b16 v18, v19 offset:1872
	ds_write_b16 v18, v19 offset:11088
	ds_write_b16 v18, v19 offset:2016
	ds_write_b16 v18, v19 offset:11232
	ds_write_b16 v18, v19 offset:2160
	ds_write_b16 v18, v19 offset:11376
	ds_write_b16 v18, v19 offset:2304
	ds_write_b16 v18, v19 offset:11520
	ds_write_b16 v18, v19 offset:2448
	ds_write_b16 v18, v19 offset:11664
	ds_write_b16 v18, v19 offset:2592
	ds_write_b16 v18, v19 offset:11808
	ds_write_b16 v18, v19 offset:2736
	ds_write_b16 v18, v19 offset:11952
	ds_write_b16 v18, v19 offset:2880
	ds_write_b16 v18, v19 offset:12096
	ds_write_b16 v18, v19 offset:3024
	ds_write_b16 v18, v19 offset:12240
	ds_write_b16 v18, v19 offset:3168
	ds_write_b16 v18, v19 offset:12384
	ds_write_b16 v18, v19 offset:3312
	ds_write_b16 v18, v19 offset:12528
	ds_write_b16 v18, v19 offset:3456
	ds_write_b16 v18, v19 offset:12672
	ds_write_b16 v18, v19 offset:3600
	ds_write_b16 v18, v19 offset:12816
	ds_write_b16 v18, v19 offset:3744
	ds_write_b16 v18, v19 offset:12960
	ds_write_b16 v18, v19 offset:3888
	ds_write_b16 v18, v19 offset:13104
	ds_write_b16 v18, v19 offset:4032
	ds_write_b16 v18, v19 offset:13248
	ds_write_b16 v18, v19 offset:4176
	ds_write_b16 v18, v19 offset:13392
	ds_write_b16 v18, v19 offset:4320
	ds_write_b16 v18, v19 offset:13536
	ds_write_b16 v18, v19 offset:4464
	ds_write_b16 v18, v19 offset:13680
	s_or_b64 exec, exec, s[12:13]
.Lg4_done:
	s_and_b32 s0, s10, 3
	s_branch .LBB0_1466
